# ssm_local: coefficient and input loads hoisted to unit top, inputs staged as f32 in LDS, hand-pipelined 21-VALU step loop
# speedup vs baseline: 1.0807x; 1.0100x over previous
.LBB0_297:
	v_ashrrev_i32_e32 v0, 31, v9
	v_lshrrev_b32_e32 v0, 27, v0
	v_add_u32_e32 v0, v9, v0
	v_ashrrev_i32_e32 v12, 5, v0
	v_mul_hi_i32 v0, v12, s78
	v_add_u32_e32 v0, v0, v12
	v_lshrrev_b32_e32 v1, 31, v0
	v_ashrrev_i32_e32 v0, 4, v0
	v_add_u32_e32 v0, v0, v1
	v_mov_b32_e32 v92, v0
	v_mul_lo_u32 v0, v0, 28
	v_sub_u32_e32 v0, v12, v0
	v_ashrrev_i32_e32 v1, 31, v0
	v_lshl_add_u64 v[2:3], v[0:1], 2, s[16:17]
	global_load_dword v1, v[2:3], off
	v_lshl_or_b32 v4, v0, 6, v8
	v_ashrrev_i32_e32 v5, 31, v4
	v_lshlrev_b64 v[6:7], 2, v[4:5]
	v_lshl_add_u64 v[2:3], s[14:15], 0, v[6:7]
	global_load_dword v3, v[2:3], off
	v_lshl_add_u64 v[6:7], s[12:13], 0, v[6:7]
	global_load_dword v2, v[6:7], off
	v_lshlrev_b64 v[88:89], 6, v[4:5]
	v_lshl_add_u64 v[90:91], s[18:19], 0, v[88:89]
	v_lshl_add_u64 v[88:89], s[20:21], 0, v[88:89]
	global_load_dwordx4 v[96:99], v[90:91], off
	global_load_dwordx4 v[100:103], v[88:89], off
	global_load_dwordx4 v[104:107], v[90:91], off offset:16
	global_load_dwordx4 v[108:111], v[88:89], off offset:16
	global_load_dwordx4 v[112:115], v[90:91], off offset:32
	global_load_dwordx4 v[116:119], v[88:89], off offset:32
	global_load_dwordx4 v[120:123], v[90:91], off offset:48
	global_load_dwordx4 v[124:127], v[88:89], off offset:48
	v_lshlrev_b32_e32 v93, 5, v12
	v_sub_u32_e32 v93, v9, v93
	v_mov_b64_e32 v[94:95], s[10:11]
	s_mov_b32 s4, 0x1060000
	s_mov_b32 s5, 0x83000
	v_mad_i64_i32 v[94:95], s[6:7], v92, s4, v[94:95]
	v_mad_i64_i32 v[94:95], s[6:7], v93, s5, v[94:95]
	v_lshlrev_b32_e32 v92, 5, v0
	v_mov_b32_e32 v93, 0
	v_lshl_add_u64 v[94:95], v[92:93], 0, v[94:95]
	v_lshl_add_u64 v[94:95], v[94:95], 0, v[10:11]
	global_load_dwordx4 v[128:131], v[94:95], off offset:2688
	global_load_dwordx4 v[132:135], v[94:95], off offset:2704
	v_lshlrev_b32_e32 v138, 1, v54
	v_lshl_add_u32 v137, v8, 6, v138
	s_waitcnt vmcnt(10) lgkmcnt(0)
	v_mul_f32_e32 v5, 0x3fb8aa3b, v1
	v_fma_f32 v6, v1, s81, -v5
	v_rndne_f32_e32 v7, v5
	v_fmac_f32_e32 v6, 0x32a5705f, v1
	v_sub_f32_e32 v5, v5, v7
	v_add_f32_e32 v5, v5, v6
	v_cvt_i32_f32_e32 v7, v7
	v_exp_f32_e32 v5, v5
	v_cmp_ngt_f32_e32 vcc, s86, v1
	v_ldexp_f32 v5, v5, v7
	s_nop 0
	v_cndmask_b32_e32 v5, 0, v5, vcc
	v_cmp_nlt_f32_e32 vcc, s92, v1
	s_nop 1
	v_cndmask_b32_e32 v1, v221, v5, vcc
	v_mul_f32_e32 v5, v3, v1
	v_and_b32_e32 v6, 0x7fffffff, v5
	v_lshrrev_b32_e32 v7, 23, v6
	v_and_b32_e32 v13, 0x7fffff, v6
	v_cmp_nlt_f32_e64 s[26:27], |v5|, s87
	v_add_u32_e32 v15, 0xffffff88, v7
	v_or_b32_e32 v14, 0x800000, v13
	s_and_saveexec_b64 s[0:1], s[26:27]
	s_xor_b64 s[28:29], exec, s[0:1]
	s_cbranch_execz .LBB0_299
	v_cmp_lt_u32_e32 vcc, 63, v15
	v_not_b32_e32 v16, 31
	v_mov_b32_e32 v19, v145
	v_cndmask_b32_e32 v7, 0, v223, vcc
	v_add_u32_e32 v7, v7, v15
	v_cmp_lt_u32_e64 s[0:1], 31, v7
	v_mov_b32_e32 v21, v145
	v_mov_b32_e32 v23, v145
	v_cndmask_b32_e64 v13, 0, v16, s[0:1]
	v_add_u32_e32 v7, v13, v7
	v_cmp_lt_u32_e64 s[4:5], 31, v7
	v_mov_b32_e32 v25, v145
	s_mov_b32 s2, 0xfc2757d1
	v_cndmask_b32_e64 v13, 0, v16, s[4:5]
	v_mad_u64_u32 v[16:17], s[6:7], v14, s88, 0
	v_mov_b32_e32 v18, v17
	v_mad_u64_u32 v[18:19], s[6:7], v14, s89, v[18:19]
	v_mov_b32_e32 v20, v19
	v_mad_u64_u32 v[20:21], s[6:7], v14, s90, v[20:21]
	v_mov_b32_e32 v22, v21
	v_mad_u64_u32 v[22:23], s[6:7], v14, s91, v[22:23]
	v_mov_b32_e32 v24, v23
	v_mad_u64_u32 v[24:25], s[6:7], v14, s2, v[24:25]
	v_mov_b32_e32 v26, v25
	v_mov_b32_e32 v27, v145
	s_mov_b32 s2, 0x4e441529
	v_mad_u64_u32 v[26:27], s[6:7], v14, s2, v[26:27]
	v_mov_b32_e32 v28, v27
	v_mov_b32_e32 v29, v145
	s_mov_b32 s2, 0xa2f9836e
	v_mad_u64_u32 v[28:29], s[6:7], v14, s2, v[28:29]
	v_add_u32_e32 v7, v13, v7
	v_cndmask_b32_e32 v13, v26, v22, vcc
	v_cndmask_b32_e32 v17, v28, v24, vcc
	v_cndmask_b32_e32 v21, v29, v26, vcc
	v_cndmask_b32_e64 v19, v17, v13, s[0:1]
	v_cndmask_b32_e64 v17, v21, v17, s[0:1]
	v_cndmask_b32_e32 v21, v24, v20, vcc
	v_cndmask_b32_e64 v13, v13, v21, s[0:1]
	v_cndmask_b32_e64 v17, v17, v19, s[4:5]
	v_cndmask_b32_e64 v19, v19, v13, s[4:5]
	v_sub_u32_e32 v23, 32, v7
	v_alignbit_b32 v24, v17, v19, v23
	v_cmp_eq_u32_e64 s[6:7], 0, v7
	v_cndmask_b32_e32 v16, v20, v16, vcc
	s_nop 0
	v_cndmask_b32_e64 v7, v24, v17, s[6:7]
	v_cndmask_b32_e32 v17, v22, v18, vcc
	v_cndmask_b32_e64 v18, v21, v17, s[0:1]
	v_cndmask_b32_e64 v13, v13, v18, s[4:5]
	v_alignbit_b32 v21, v19, v13, v23
	v_cndmask_b32_e64 v19, v21, v19, s[6:7]
	v_bfe_u32 v24, v7, 29, 1
	v_cndmask_b32_e64 v16, v17, v16, s[0:1]
	v_alignbit_b32 v21, v7, v19, 30
	v_sub_u32_e32 v25, 0, v24
	v_cndmask_b32_e64 v16, v18, v16, s[4:5]
	v_xor_b32_e32 v21, v21, v25
	v_alignbit_b32 v17, v13, v16, v23
	v_cndmask_b32_e64 v13, v17, v13, s[6:7]
	v_ffbh_u32_e32 v18, v21
	v_alignbit_b32 v17, v19, v13, 30
	v_min_u32_e32 v18, 32, v18
	v_alignbit_b32 v13, v13, v16, 30
	v_xor_b32_e32 v17, v17, v25
	v_sub_u32_e32 v19, 31, v18
	v_xor_b32_e32 v13, v13, v25
	v_alignbit_b32 v20, v21, v17, v19
	v_alignbit_b32 v13, v17, v13, v19
	v_alignbit_b32 v16, v20, v13, 9
	v_ffbh_u32_e32 v17, v16
	v_min_u32_e32 v17, 32, v17
	v_lshrrev_b32_e32 v22, 29, v7
	v_not_b32_e32 v19, v17
	v_alignbit_b32 v13, v16, v13, v19
	v_lshlrev_b32_e32 v16, 31, v22
	v_or_b32_e32 v19, 0x33000000, v16
	v_add_lshl_u32 v17, v17, v18, 23
	v_lshrrev_b32_e32 v13, 9, v13
	v_sub_u32_e32 v17, v19, v17
	v_or_b32_e32 v16, 0.5, v16
	v_lshlrev_b32_e32 v18, 23, v18
	v_or_b32_e32 v13, v17, v13
	v_lshrrev_b32_e32 v17, 9, v20
	v_sub_u32_e32 v16, v16, v18
	v_or_b32_e32 v16, v17, v16
	v_mul_f32_e32 v17, 0x3fc90fda, v16
	s_mov_b32 s0, 0x3fc90fda
	v_fma_f32 v18, v16, s0, -v17
	v_fmac_f32_e32 v18, 0x33a22168, v16
	v_fmac_f32_e32 v18, 0x3fc90fda, v13
	v_lshrrev_b32_e32 v7, 30, v7
	v_add_f32_e32 v13, v17, v18
	v_add_u32_e32 v7, v24, v7

.LBB0_305:
	s_or_b64 exec, exec, s[0:1]
	v_mul_f32_e32 v1, v2, v1
	v_mul_f32_e32 v14, 0x3fb8aa3b, v1
	v_fma_f32 v15, v1, s81, -v14
	v_rndne_f32_e32 v16, v14
	v_fmac_f32_e32 v15, 0x32a5705f, v1
	v_sub_f32_e32 v14, v14, v16
	v_add_f32_e32 v14, v14, v15
	v_exp_f32_e32 v14, v14
	v_cvt_i32_f32_e32 v15, v16
	v_cmp_ngt_f32_e32 vcc, s86, v1
	s_brev_b32 s0, 1
	v_mov_b32_e32 v20, 0x7fc00000
	v_ldexp_f32 v14, v14, v15
	v_cndmask_b32_e32 v14, 0, v14, vcc
	v_cmp_nlt_f32_e32 vcc, s92, v1
	v_mul_f32_e32 v1, v13, v13
	v_lshlrev_b32_e32 v4, 4, v4
	v_cndmask_b32_e32 v15, v221, v14, vcc
	v_fmamk_f32 v14, v1, 0xb94c1982, v253
	v_fmaak_f32 v14, v1, v14, 0xbe2aaa9d
	v_mul_f32_e32 v14, v1, v14
	v_fmac_f32_e32 v13, v13, v14
	v_fmamk_f32 v14, v1, 0x37d75334, v222
	v_fmaak_f32 v14, v1, v14, 0x3d2aabf7
	v_fmaak_f32 v14, v1, v14, 0xbf000004
	v_fma_f32 v1, v1, v14, 1.0
	v_and_b32_e32 v14, 1, v7
	v_cmp_eq_u32_e32 vcc, 0, v14
	v_lshlrev_b32_e32 v7, 30, v7
	v_lshlrev_b32_e32 v0, 4, v0
	v_cndmask_b32_e64 v1, -v13, v1, vcc
	v_bitop3_b32 v1, v7, v1, s0 bitop3:0x6c
	s_movk_i32 s0, 0x1f8
	v_cmp_class_f32_e64 vcc, v5, s0
	v_xor_b32_e32 v5, v6, v5
	v_mov_b32_e32 v52, 0
	v_cndmask_b32_e32 v7, v20, v1, vcc
	v_lshlrev_b32_e32 v1, 5, v12
	v_sub_u32_e32 v14, v9, v1
	v_mul_hi_i32 v1, v9, s78
	v_add_u32_e32 v1, v1, v9
	v_lshrrev_b32_e32 v13, 31, v1
	v_ashrrev_i32_e32 v1, 9, v1
	v_add_u32_e32 v1, v1, v13
	v_mul_f32_e32 v13, v18, v18
	v_fmamk_f32 v19, v13, 0xb94c1982, v253
	v_fmaak_f32 v19, v13, v19, 0xbe2aaa9d
	v_mul_f32_e32 v19, v13, v19
	v_fmac_f32_e32 v18, v18, v19
	v_fmamk_f32 v19, v13, 0x37d75334, v222
	v_fmaak_f32 v19, v13, v19, 0x3d2aabf7
	v_fmaak_f32 v19, v13, v19, 0xbf000004
	v_fma_f32 v13, v13, v19, 1.0
	v_and_b32_e32 v19, 1, v17
	v_lshlrev_b32_e32 v17, 30, v17
	v_cmp_eq_u32_e64 s[0:1], 0, v19
	v_and_b32_e32 v17, 0x80000000, v17
	v_xor_b32_e32 v5, v5, v17
	v_cndmask_b32_e64 v13, v13, v18, s[0:1]
	v_xor_b32_e32 v5, v5, v13
	v_cndmask_b32_e32 v5, v20, v5, vcc
	v_mul_f32_e32 v18, v15, v5
	v_ashrrev_i32_e32 v5, 31, v4
	v_lshlrev_b64 v[4:5], 2, v[4:5]
	v_lshl_add_u64 v[20:21], s[18:19], 0, v[4:5]
	v_lshl_add_u64 v[4:5], s[20:21], 0, v[4:5]
	s_waitcnt vmcnt(2)
	v_mov_b64_e32 v[24:25], v[96:97]
	v_mov_b64_e32 v[26:27], v[98:99]
	v_mov_b64_e32 v[28:29], v[100:101]
	v_mov_b64_e32 v[30:31], v[102:103]
	v_mov_b64_e32 v[32:33], v[104:105]
	v_mov_b64_e32 v[34:35], v[106:107]
	v_mov_b64_e32 v[36:37], v[108:109]
	v_mov_b64_e32 v[38:39], v[110:111]
	v_mov_b64_e32 v[40:41], v[112:113]
	v_mov_b64_e32 v[42:43], v[114:115]
	v_mov_b64_e32 v[44:45], v[116:117]
	v_mov_b64_e32 v[46:47], v[118:119]
	v_mov_b64_e32 v[48:49], v[120:121]
	v_mov_b64_e32 v[50:51], v[122:123]
	v_mov_b64_e32 v[56:57], v[124:125]
	v_mov_b64_e32 v[58:59], v[126:127]
	v_fma_f32 v19, v15, v7, -1.0
	v_mov_b32_e32 v4, v3
	v_mul_f32_e32 v16, v15, v7
	v_pk_mul_f32 v[6:7], v[2:3], v[2:3]
	v_pk_mul_f32 v[4:5], v[4:5], v[18:19] op_sel:[0,1] op_sel_hi:[0,0]
	v_pk_fma_f32 v[20:21], v[2:3], v[18:19], v[4:5] op_sel_hi:[0,1,1]
	v_pk_fma_f32 v[2:3], v[2:3], v[18:19], v[4:5] op_sel_hi:[0,1,1] neg_lo:[0,0,1] neg_hi:[0,0,1]
	v_pk_add_f32 v[4:5], v[6:7], v[6:7] op_sel:[0,1] op_sel_hi:[0,1]
	v_div_scale_f32 v3, s[0:1], v5, v5, v21
	v_rcp_f32_e32 v6, v3
	s_mov_b32 s4, 0
	v_xor_b32_e32 v19, 0x80000000, v18
	v_mov_b32_e32 v17, v16
	v_fma_f32 v7, -v3, v6, 1.0
	v_fmac_f32_e32 v6, v7, v6
	v_div_scale_f32 v7, vcc, v21, v5, v21
	v_mul_f32_e32 v13, v7, v6
	v_fma_f32 v15, -v3, v13, v7
	v_fmac_f32_e32 v13, v15, v6
	v_fma_f32 v3, -v3, v13, v7
	v_div_fmas_f32 v3, v3, v6, v13
	v_div_fixup_f32 v3, v3, v5, v21
	v_div_scale_f32 v5, s[0:1], v4, v4, v2
	v_rcp_f32_e32 v6, v5
	s_mov_b32 s0, 0x1060000
	v_mov_b32_e32 v53, v52
	v_fma_f32 v7, -v5, v6, 1.0
	v_fmac_f32_e32 v6, v7, v6
	v_div_scale_f32 v7, vcc, v2, v4, v2
	v_mul_f32_e32 v13, v7, v6
	v_fma_f32 v15, -v5, v13, v7
	v_fmac_f32_e32 v13, v15, v6
	v_fma_f32 v5, -v5, v13, v7
	v_div_fmas_f32 v5, v5, v6, v13
	v_div_fixup_f32 v2, v5, v4, v2
	v_ashrrev_i32_e32 v15, 31, v14
	s_waitcnt vmcnt(0) lgkmcnt(0)
	v_pk_mul_f32 v[4:5], v[28:29], v[2:3] op_sel:[0,1] op_sel_hi:[0,0]
	v_pk_fma_f32 v[6:7], v[24:25], v[2:3], v[4:5] op_sel_hi:[0,1,1] neg_lo:[0,0,1] neg_hi:[0,0,1]
	v_pk_fma_f32 v[20:21], v[24:25], v[2:3], v[4:5] op_sel_hi:[0,1,1]
	v_pk_mul_f32 v[4:5], v[28:29], v[2:3] op_sel:[1,1] op_sel_hi:[1,0]
	v_mov_b32_e32 v21, v7
	v_pk_fma_f32 v[6:7], v[24:25], v[2:3], v[4:5] op_sel:[1,0,0] neg_lo:[0,0,1] neg_hi:[0,0,1]
	v_pk_fma_f32 v[22:23], v[24:25], v[2:3], v[4:5] op_sel:[1,0,0]
	v_pk_mul_f32 v[4:5], v[30:31], v[2:3] op_sel:[0,1] op_sel_hi:[0,0]
	v_mov_b32_e32 v23, v7
	v_pk_fma_f32 v[6:7], v[26:27], v[2:3], v[4:5] op_sel_hi:[0,1,1] neg_lo:[0,0,1] neg_hi:[0,0,1]
	v_pk_fma_f32 v[24:25], v[26:27], v[2:3], v[4:5] op_sel_hi:[0,1,1]
	v_mov_b32_e32 v4, v31
	v_pk_mul_f32 v[4:5], v[4:5], v[2:3] op_sel:[0,1] op_sel_hi:[0,0]
	v_mov_b32_e32 v6, v27
	v_pk_fma_f32 v[28:29], v[6:7], v[2:3], v[4:5] op_sel_hi:[0,1,1] neg_lo:[0,0,1] neg_hi:[0,0,1]
	v_pk_fma_f32 v[26:27], v[6:7], v[2:3], v[4:5] op_sel_hi:[0,1,1]
	v_pk_mul_f32 v[4:5], v[2:3], v[36:37] op_sel:[1,0] op_sel_hi:[0,0]
	v_mov_b32_e32 v25, v7
	v_mov_b32_e32 v27, v29
	v_pk_fma_f32 v[6:7], v[32:33], v[2:3], v[4:5] op_sel_hi:[0,1,1] neg_lo:[0,0,1] neg_hi:[0,0,1]
	v_pk_fma_f32 v[28:29], v[32:33], v[2:3], v[4:5] op_sel_hi:[0,1,1]
	v_pk_mul_f32 v[4:5], v[2:3], v[36:37] op_sel:[1,1] op_sel_hi:[0,1]
	v_mov_b32_e32 v29, v7
	v_pk_fma_f32 v[6:7], v[32:33], v[2:3], v[4:5] op_sel:[1,0,0] neg_lo:[0,0,1] neg_hi:[0,0,1]
	v_pk_fma_f32 v[30:31], v[32:33], v[2:3], v[4:5] op_sel:[1,0,0]
	v_pk_mul_f32 v[4:5], v[2:3], v[38:39] op_sel:[1,0] op_sel_hi:[0,0]
	v_mov_b32_e32 v31, v7
	v_pk_fma_f32 v[6:7], v[34:35], v[2:3], v[4:5] op_sel_hi:[0,1,1] neg_lo:[0,0,1] neg_hi:[0,0,1]
	v_pk_fma_f32 v[32:33], v[34:35], v[2:3], v[4:5] op_sel_hi:[0,1,1]
	v_mov_b32_e32 v4, v39
	v_pk_mul_f32 v[4:5], v[2:3], v[4:5] op_sel:[1,0] op_sel_hi:[0,0]
	v_mov_b32_e32 v6, v35
	v_pk_fma_f32 v[36:37], v[6:7], v[2:3], v[4:5] op_sel_hi:[0,1,1] neg_lo:[0,0,1] neg_hi:[0,0,1]
	v_pk_fma_f32 v[34:35], v[6:7], v[2:3], v[4:5] op_sel_hi:[0,1,1]
	v_pk_mul_f32 v[4:5], v[2:3], v[44:45] op_sel:[1,0] op_sel_hi:[0,0]
	v_mov_b32_e32 v33, v7
	v_mov_b32_e32 v35, v37
	v_pk_fma_f32 v[6:7], v[2:3], v[40:41], v[4:5] op_sel_hi:[1,0,1] neg_lo:[0,0,1] neg_hi:[0,0,1]
	v_pk_fma_f32 v[36:37], v[2:3], v[40:41], v[4:5] op_sel_hi:[1,0,1]
	v_pk_mul_f32 v[4:5], v[2:3], v[44:45] op_sel:[1,1] op_sel_hi:[0,1]
	v_mov_b32_e32 v37, v7
	v_pk_fma_f32 v[6:7], v[2:3], v[40:41], v[4:5] op_sel:[0,1,0] neg_lo:[0,0,1] neg_hi:[0,0,1]
	v_pk_fma_f32 v[38:39], v[2:3], v[40:41], v[4:5] op_sel:[0,1,0]
	v_pk_mul_f32 v[4:5], v[2:3], v[46:47] op_sel:[1,0] op_sel_hi:[0,0]
	v_mov_b32_e32 v39, v7
	v_pk_fma_f32 v[6:7], v[2:3], v[42:43], v[4:5] op_sel_hi:[1,0,1] neg_lo:[0,0,1] neg_hi:[0,0,1]
	v_pk_fma_f32 v[40:41], v[2:3], v[42:43], v[4:5] op_sel_hi:[1,0,1]
	v_mov_b32_e32 v4, v47
	v_pk_mul_f32 v[4:5], v[2:3], v[4:5] op_sel:[1,0] op_sel_hi:[0,0]
	v_mov_b32_e32 v6, v43
	v_pk_fma_f32 v[44:45], v[2:3], v[6:7], v[4:5] op_sel_hi:[1,0,1] neg_lo:[0,0,1] neg_hi:[0,0,1]
	v_pk_fma_f32 v[42:43], v[2:3], v[6:7], v[4:5] op_sel_hi:[1,0,1]
	v_pk_mul_f32 v[4:5], v[2:3], v[56:57] op_sel:[1,0] op_sel_hi:[0,0]
	v_mov_b32_e32 v41, v7
	v_mov_b32_e32 v43, v45
	v_pk_fma_f32 v[6:7], v[2:3], v[48:49], v[4:5] op_sel_hi:[1,0,1] neg_lo:[0,0,1] neg_hi:[0,0,1]
	v_pk_fma_f32 v[44:45], v[2:3], v[48:49], v[4:5] op_sel_hi:[1,0,1]
	v_pk_mul_f32 v[4:5], v[2:3], v[56:57] op_sel:[1,1] op_sel_hi:[0,1]
	v_mov_b32_e32 v45, v7
	v_pk_fma_f32 v[6:7], v[2:3], v[48:49], v[4:5] op_sel:[0,1,0] neg_lo:[0,0,1] neg_hi:[0,0,1]
	v_pk_fma_f32 v[46:47], v[2:3], v[48:49], v[4:5] op_sel:[0,1,0]
	v_pk_mul_f32 v[4:5], v[2:3], v[58:59] op_sel:[1,0] op_sel_hi:[0,0]
	v_mov_b32_e32 v47, v7
	v_pk_fma_f32 v[6:7], v[2:3], v[50:51], v[4:5] op_sel_hi:[1,0,1] neg_lo:[0,0,1] neg_hi:[0,0,1]
	v_pk_fma_f32 v[48:49], v[2:3], v[50:51], v[4:5] op_sel_hi:[1,0,1]
	v_mov_b32_e32 v4, v59
	v_pk_mul_f32 v[4:5], v[2:3], v[4:5] op_sel:[1,0] op_sel_hi:[0,0]
	v_mov_b32_e32 v6, v51
	v_pk_fma_f32 v[56:57], v[2:3], v[6:7], v[4:5] op_sel_hi:[1,0,1] neg_lo:[0,0,1] neg_hi:[0,0,1]
	v_pk_fma_f32 v[50:51], v[2:3], v[6:7], v[4:5] op_sel_hi:[1,0,1]
	v_mov_b64_e32 v[2:3], s[10:11]
	v_mad_i64_i32 v[2:3], s[0:1], v1, s0, v[2:3]
	s_mov_b32 s0, 0x83000
	s_nop 0
	v_mad_i64_i32 v[2:3], s[0:1], v14, s0, v[2:3]
	v_ashrrev_i32_e32 v1, 31, v0
	v_lshl_add_u64 v[0:1], v[0:1], 1, v[2:3]
	v_lshl_add_u64 v[4:5], v[0:1], 0, v[10:11]
	v_mov_b32_e32 v49, v7
	s_waitcnt vmcnt(0)
	v_lshlrev_b32_e32 v146, 16, v128
	v_and_b32_e32 v147, 0xffff0000, v128
	v_lshlrev_b32_e32 v148, 16, v129
	v_and_b32_e32 v149, 0xffff0000, v129
	v_lshlrev_b32_e32 v150, 16, v130
	v_and_b32_e32 v151, 0xffff0000, v130
	v_lshlrev_b32_e32 v152, 16, v131
	v_and_b32_e32 v153, 0xffff0000, v131
	v_lshlrev_b32_e32 v154, 16, v132
	v_and_b32_e32 v155, 0xffff0000, v132
	v_lshlrev_b32_e32 v156, 16, v133
	v_and_b32_e32 v157, 0xffff0000, v133
	v_lshlrev_b32_e32 v158, 16, v134
	v_and_b32_e32 v159, 0xffff0000, v134
	v_lshlrev_b32_e32 v160, 16, v135
	v_and_b32_e32 v161, 0xffff0000, v135
	ds_write_b128 v137, v[146:149]
	ds_write_b128 v137, v[150:153] offset:16
	ds_write_b128 v137, v[154:157] offset:32
	ds_write_b128 v137, v[158:161] offset:48
	v_mov_b32_e32 v51, v57
	s_waitcnt lgkmcnt(0)
	ds_read_b128 v[146:149], v138
	ds_read_b128 v[150:153], v138 offset:16
	ds_read_b128 v[154:157], v138 offset:32
	ds_read_b128 v[158:161], v138 offset:48
	v_mov_b64_e32 v[60:61], 0
	v_mov_b64_e32 v[62:63], 0
	v_mov_b64_e32 v[64:65], 0
	v_mov_b64_e32 v[66:67], 0
	s_mov_b32 s4, 0
.Lssml_loop:
	ds_read_b128 v[162:165], v138 offset:64
	ds_read_b128 v[166:169], v138 offset:80
	ds_read_b128 v[170:173], v138 offset:96
	ds_read_b128 v[174:177], v138 offset:112
	s_waitcnt lgkmcnt(4)
	v_pk_fma_f32 v[0:1], v[146:147], v[20:21], 0 op_sel_hi:[0,1,0]
	v_pk_add_f32 v[60:61], v[60:61], v[62:63]
	v_pk_fma_f32 v[2:3], v[146:147], v[22:23], 0 op_sel:[1,0,0] op_sel_hi:[1,1,0]
	v_pk_add_f32 v[64:65], v[64:65], v[66:67]
	v_pk_fma_f32 v[4:5], v[148:149], v[24:25], 0 op_sel_hi:[0,1,0]
	v_pk_add_f32 v[60:61], v[60:61], v[64:65]
	v_pk_fma_f32 v[6:7], v[148:149], v[26:27], 0 op_sel:[1,0,0] op_sel_hi:[1,1,0]
	v_pk_fma_f32 v[60:61], v[18:19], v[52:53], v[60:61] op_sel:[0,1,0] op_sel_hi:[1,0,1]
	v_pk_fma_f32 v[0:1], v[150:151], v[28:29], v[0:1] op_sel_hi:[0,1,1]
	v_pk_fma_f32 v[52:53], v[16:17], v[52:53], v[60:61]
	v_pk_fma_f32 v[2:3], v[150:151], v[30:31], v[2:3] op_sel:[1,0,0]
	v_pk_fma_f32 v[4:5], v[152:153], v[32:33], v[4:5] op_sel_hi:[0,1,1]
	v_pk_fma_f32 v[6:7], v[152:153], v[34:35], v[6:7] op_sel:[1,0,0]
	v_pk_fma_f32 v[0:1], v[154:155], v[36:37], v[0:1] op_sel_hi:[0,1,1]
	v_pk_fma_f32 v[2:3], v[154:155], v[38:39], v[2:3] op_sel:[1,0,0]
	v_pk_fma_f32 v[4:5], v[156:157], v[40:41], v[4:5] op_sel_hi:[0,1,1]
	v_pk_fma_f32 v[6:7], v[156:157], v[42:43], v[6:7] op_sel:[1,0,0]
	v_pk_fma_f32 v[0:1], v[158:159], v[44:45], v[0:1] op_sel_hi:[0,1,1]
	v_pk_fma_f32 v[2:3], v[158:159], v[46:47], v[2:3] op_sel:[1,0,0]
	v_pk_fma_f32 v[4:5], v[160:161], v[48:49], v[4:5] op_sel_hi:[0,1,1]
	v_pk_fma_f32 v[6:7], v[160:161], v[50:51], v[6:7] op_sel:[1,0,0]
	ds_read_b128 v[146:149], v138 offset:128
	ds_read_b128 v[150:153], v138 offset:144
	ds_read_b128 v[154:157], v138 offset:160
	ds_read_b128 v[158:161], v138 offset:176
	s_waitcnt lgkmcnt(4)
	v_pk_fma_f32 v[60:61], v[162:163], v[20:21], 0 op_sel_hi:[0,1,0]
	v_pk_add_f32 v[0:1], v[0:1], v[2:3]
	v_pk_fma_f32 v[62:63], v[162:163], v[22:23], 0 op_sel:[1,0,0] op_sel_hi:[1,1,0]
	v_pk_add_f32 v[4:5], v[4:5], v[6:7]
	v_pk_fma_f32 v[64:65], v[164:165], v[24:25], 0 op_sel_hi:[0,1,0]
	v_pk_add_f32 v[0:1], v[0:1], v[4:5]
	v_pk_fma_f32 v[66:67], v[164:165], v[26:27], 0 op_sel:[1,0,0] op_sel_hi:[1,1,0]
	v_pk_fma_f32 v[0:1], v[18:19], v[52:53], v[0:1] op_sel:[0,1,0] op_sel_hi:[1,0,1]
	v_pk_fma_f32 v[60:61], v[166:167], v[28:29], v[60:61] op_sel_hi:[0,1,1]
	v_pk_fma_f32 v[52:53], v[16:17], v[52:53], v[0:1]
	v_pk_fma_f32 v[62:63], v[166:167], v[30:31], v[62:63] op_sel:[1,0,0]
	v_pk_fma_f32 v[64:65], v[168:169], v[32:33], v[64:65] op_sel_hi:[0,1,1]
	v_pk_fma_f32 v[66:67], v[168:169], v[34:35], v[66:67] op_sel:[1,0,0]
	v_pk_fma_f32 v[60:61], v[170:171], v[36:37], v[60:61] op_sel_hi:[0,1,1]
	v_pk_fma_f32 v[62:63], v[170:171], v[38:39], v[62:63] op_sel:[1,0,0]
	v_pk_fma_f32 v[64:65], v[172:173], v[40:41], v[64:65] op_sel_hi:[0,1,1]
	v_pk_fma_f32 v[66:67], v[172:173], v[42:43], v[66:67] op_sel:[1,0,0]
	v_pk_fma_f32 v[60:61], v[174:175], v[44:45], v[60:61] op_sel_hi:[0,1,1]
	v_pk_fma_f32 v[62:63], v[174:175], v[46:47], v[62:63] op_sel:[1,0,0]
	v_pk_fma_f32 v[64:65], v[176:177], v[48:49], v[64:65] op_sel_hi:[0,1,1]
	v_pk_fma_f32 v[66:67], v[176:177], v[50:51], v[66:67] op_sel:[1,0,0]
	v_add_u32_e32 v138, 0x80, v138
	s_add_i32 s4, s4, 1
	s_cmp_eq_u32 s4, 32
	s_cbranch_scc0 .Lssml_loop
	v_pk_add_f32 v[60:61], v[60:61], v[62:63]
	v_pk_add_f32 v[64:65], v[64:65], v[66:67]
	s_nop 0
	v_pk_add_f32 v[60:61], v[60:61], v[64:65]
	s_nop 0
	v_pk_fma_f32 v[60:61], v[18:19], v[52:53], v[60:61] op_sel:[0,1,0] op_sel_hi:[1,0,1]
	s_nop 0
	v_pk_fma_f32 v[52:53], v[16:17], v[52:53], v[60:61]
	v_ashrrev_i32_e32 v13, 31, v12
	v_lshlrev_b64 v[0:1], 14, v[12:13]
	v_lshl_add_u64 v[0:1], s[22:23], 0, v[0:1]
	v_lshlrev_b64 v[2:3], 9, v[14:15]
	v_lshl_add_u64 v[0:1], v[0:1], 0, v[2:3]
	s_waitcnt lgkmcnt(0)
	v_lshl_add_u64 v[0:1], v[0:1], 0, v[144:145]
	s_movk_i32 s0, 0x5ff
	global_store_dword v[0:1], v53, off
	global_store_dword v[0:1], v52, off offset:256
	v_add_u32_e32 v0, 0x800, v9
	v_cmp_lt_i32_e32 vcc, s0, v9
	s_or_b64 s[24:25], vcc, s[24:25]
	v_mov_b32_e32 v9, v0
	s_andn2_b64 exec, exec, s[24:25]
	s_cbranch_execnz .LBB0_297
